# baseline (speedup 1.0000x reference)
.Llight_loop:
	v_mfma_f32_32x32x16_bf16 v[18:33], v[78:81], v[130:133], v[18:33]
	ds_read_b128 v[162:165], v210 offset:8192
	ds_read_b128 v[166:169], v210 offset:9216
	ds_read_b128 v[82:85], v234 offset:128
	ds_read_b128 v[86:89], v234 offset:144
	ds_read_b128 v[90:93], v234 offset:160
	ds_read_b128 v[94:97], v234 offset:176
	ds_read2_b32 v[244:245], v232 offset1:32
	v_exp_f32_e32 v212, v4
	v_exp_f32_e32 v213, v8
	v_exp_f32_e32 v214, v12
	v_exp_f32_e32 v215, v16
	v_mfma_f32_32x32x16_bf16 v[18:33], v[74:77], v[134:137], v[18:33]
	ds_read_b128 v[170:173], v210 offset:10240
	ds_read_b128 v[174:177], v210 offset:11264
	v_exp_f32_e32 v217, v2
	v_fma_f32 v251, v212, s12, s12
	v_exp_f32_e32 v218, v6
	v_fma_f32 v252, v213, s12, s12
	v_exp_f32_e32 v219, v10
	v_fma_f32 v253, v214, s12, s12
	v_exp_f32_e32 v220, v14
	v_fma_f32 v254, v215, s12, s12
	v_mfma_f32_32x32x16_bf16 v[18:33], v[70:73], v[138:141], v[18:33]
	ds_read_b128 v[178:181], v210 offset:12288
	ds_read_b128 v[182:185], v210 offset:13312
	v_exp_f32_e32 v221, v3
	v_fmac_f32_e32 v251, v217, v251
	v_exp_f32_e32 v222, v7
	v_fmac_f32_e32 v252, v218, v252
	v_exp_f32_e32 v223, v11
	v_fmac_f32_e32 v253, v219, v253
	v_exp_f32_e32 v224, v15
	v_fmac_f32_e32 v254, v220, v254
	v_mfma_f32_32x32x16_bf16 v[18:33], v[66:69], v[142:145], v[18:33]
	ds_read_b128 v[186:189], v210 offset:14336
	ds_read_b128 v[190:193], v210 offset:15360
	v_rcp_f32_e32 v217, v251
	v_add_f32_e32 v221, 1.0, v221
	v_rcp_f32_e32 v218, v252
	v_add_f32_e32 v222, 1.0, v222
	v_rcp_f32_e32 v219, v253
	v_add_f32_e32 v223, 1.0, v223
	v_rcp_f32_e32 v220, v254
	v_add_f32_e32 v224, 1.0, v224
	v_mfma_f32_32x32x16_bf16 v[18:33], v[62:65], v[146:149], v[18:33]
	v_rcp_f32_e32 v221, v221
	v_fma_f32 v240, -v212, v217, v217
	v_rcp_f32_e32 v222, v222
	v_fma_f32 v241, -v213, v218, v218
	v_rcp_f32_e32 v223, v223
	v_fma_f32 v242, -v214, v219, v219
	v_rcp_f32_e32 v224, v224
	v_fma_f32 v243, -v215, v220, v220
	v_mfma_f32_32x32x16_bf16 v[18:33], v[58:61], v[150:153], v[18:33]
	v_exp_f32_e32 v246, v5
	v_fma_f32 v194, v221, v194, v240
	v_exp_f32_e32 v247, v9
	v_fma_f32 v195, v222, v195, v241
	v_exp_f32_e32 v248, v13
	v_fma_f32 v196, v223, v196, v242
	v_exp_f32_e32 v249, v17
	v_fma_f32 v197, v224, v197, v243
	v_mfma_f32_32x32x16_bf16 v[18:33], v[54:57], v[154:157], v[18:33]
	v_exp_f32_e32 v212, v194
	v_add_f32_e32 v246, 1.0, v246
	v_exp_f32_e32 v213, v195
	v_add_f32_e32 v247, 1.0, v247
	v_exp_f32_e32 v214, v196
	v_add_f32_e32 v248, 1.0, v248
	v_exp_f32_e32 v215, v197
	v_add_f32_e32 v249, 1.0, v249
	v_fmac_f32_e32 v246, v246, v212
	v_fmac_f32_e32 v247, v247, v213
	v_fmac_f32_e32 v248, v248, v214
	v_fmac_f32_e32 v249, v249, v215
	v_mfma_f32_32x32x16_bf16 v[18:33], v[50:53], v[158:161], v[18:33]
	v_rcp_f32_e32 v246, v246
	v_rcp_f32_e32 v247, v247
	v_rcp_f32_e32 v248, v248
	v_rcp_f32_e32 v249, v249
	v_fma_f32 v246, -v212, v246, v246
	v_fma_f32 v247, -v213, v247, v247
	v_fma_f32 v248, -v214, v248, v248
	v_fma_f32 v249, -v215, v249, v249
	v_cvt_pk_bf16_f32 v236, v246, v247
	v_cvt_pk_bf16_f32 v237, v248, v249
	s_waitcnt lgkmcnt(0)
	v_mfma_f32_32x32x16_bf16 v[34:49], v[126:129], v[162:165], v[34:49]
	v_add_u32_e32 v233, v231, v244
	ds_read_b128 v[2:5], v233 offset:0
	ds_read_b128 v[6:9], v233 offset:16
	ds_read_b128 v[10:13], v233 offset:32
	ds_read_b128 v[14:17], v233 offset:48
	v_exp_f32_e32 v212, v20
	v_exp_f32_e32 v213, v24
	v_exp_f32_e32 v214, v28
	v_exp_f32_e32 v215, v32
	v_mfma_f32_32x32x16_bf16 v[34:49], v[122:125], v[166:169], v[34:49]
	v_exp_f32_e32 v217, v18
	v_fma_f32 v251, v212, s12, s12
	v_exp_f32_e32 v218, v22
	v_fma_f32 v252, v213, s12, s12
	v_exp_f32_e32 v219, v26
	v_fma_f32 v253, v214, s12, s12
	v_exp_f32_e32 v220, v30
	v_fma_f32 v254, v215, s12, s12
	v_mfma_f32_32x32x16_bf16 v[34:49], v[118:121], v[170:173], v[34:49]
	v_exp_f32_e32 v221, v19
	v_fmac_f32_e32 v251, v217, v251
	v_exp_f32_e32 v222, v23
	v_fmac_f32_e32 v252, v218, v252
	v_exp_f32_e32 v223, v27
	v_fmac_f32_e32 v253, v219, v253
	v_exp_f32_e32 v224, v31
	v_fmac_f32_e32 v254, v220, v254
	v_mfma_f32_32x32x16_bf16 v[34:49], v[114:117], v[174:177], v[34:49]
	v_rcp_f32_e32 v217, v251
	v_add_f32_e32 v221, 1.0, v221
	v_rcp_f32_e32 v218, v252
	v_add_f32_e32 v222, 1.0, v222
	v_rcp_f32_e32 v219, v253
	v_add_f32_e32 v223, 1.0, v223
	v_rcp_f32_e32 v220, v254
	v_add_f32_e32 v224, 1.0, v224
	v_mfma_f32_32x32x16_bf16 v[34:49], v[110:113], v[178:181], v[34:49]
	v_rcp_f32_e32 v221, v221
	v_fma_f32 v240, -v212, v217, v217
	v_rcp_f32_e32 v222, v222
	v_fma_f32 v241, -v213, v218, v218
	v_rcp_f32_e32 v223, v223
	v_fma_f32 v242, -v214, v219, v219
	v_rcp_f32_e32 v224, v224
	v_fma_f32 v243, -v215, v220, v220
	v_mfma_f32_32x32x16_bf16 v[34:49], v[106:109], v[182:185], v[34:49]
	v_exp_f32_e32 v246, v21
	v_fma_f32 v198, v221, v198, v240
	v_exp_f32_e32 v247, v25
	v_fma_f32 v199, v222, v199, v241
	v_exp_f32_e32 v248, v29
	v_fma_f32 v200, v223, v200, v242
	v_exp_f32_e32 v249, v33
	v_fma_f32 v201, v224, v201, v243
	v_mfma_f32_32x32x16_bf16 v[34:49], v[102:105], v[186:189], v[34:49]
	v_exp_f32_e32 v212, v198
	v_add_f32_e32 v246, 1.0, v246
	v_exp_f32_e32 v213, v199
	v_add_f32_e32 v247, 1.0, v247
	v_exp_f32_e32 v214, v200
	v_add_f32_e32 v248, 1.0, v248
	v_exp_f32_e32 v215, v201
	v_add_f32_e32 v249, 1.0, v249
	v_fmac_f32_e32 v246, v246, v212
	v_fmac_f32_e32 v247, v247, v213
	v_fmac_f32_e32 v248, v248, v214
	v_fmac_f32_e32 v249, v249, v215
	v_mfma_f32_32x32x16_bf16 v[34:49], v[98:101], v[190:193], v[34:49]
	v_rcp_f32_e32 v246, v246
	v_rcp_f32_e32 v247, v247
	v_rcp_f32_e32 v248, v248
	v_rcp_f32_e32 v249, v249
	v_fma_f32 v246, -v212, v246, v246
	v_fma_f32 v247, -v213, v247, v247
	v_fma_f32 v248, -v214, v248, v248
	v_fma_f32 v249, -v215, v249, v249
	v_cvt_pk_bf16_f32 v238, v246, v247
	v_cvt_pk_bf16_f32 v239, v248, v249
	ds_write_b128 v211, v[236:239] offset:0
	s_waitcnt lgkmcnt(0)
	s_barrier
	v_mfma_f32_32x32x16_bf16 v[82:97], v[78:81], v[162:165], v[82:97]
	ds_read_b128 v[130:133], v210 offset:0
	ds_read_b128 v[134:137], v210 offset:1024
	ds_read_b128 v[18:21], v233 offset:128
	ds_read_b128 v[22:25], v233 offset:144
	ds_read_b128 v[26:29], v233 offset:160
	ds_read_b128 v[30:33], v233 offset:176
	v_exp_f32_e32 v212, v36
	v_exp_f32_e32 v213, v40
	v_exp_f32_e32 v214, v44
	v_exp_f32_e32 v215, v48
	v_mfma_f32_32x32x16_bf16 v[82:97], v[74:77], v[166:169], v[82:97]
	ds_read_b128 v[138:141], v210 offset:2048
	ds_read_b128 v[142:145], v210 offset:3072
	v_exp_f32_e32 v217, v34
	v_fma_f32 v251, v212, s12, s12
	v_exp_f32_e32 v218, v38
	v_fma_f32 v252, v213, s12, s12
	v_exp_f32_e32 v219, v42
	v_fma_f32 v253, v214, s12, s12
	v_exp_f32_e32 v220, v46
	v_fma_f32 v254, v215, s12, s12
	v_mfma_f32_32x32x16_bf16 v[82:97], v[70:73], v[170:173], v[82:97]
	ds_read_b128 v[146:149], v210 offset:4096
	ds_read_b128 v[150:153], v210 offset:5120
	v_exp_f32_e32 v221, v35
	v_fmac_f32_e32 v251, v217, v251
	v_exp_f32_e32 v222, v39
	v_fmac_f32_e32 v252, v218, v252
	v_exp_f32_e32 v223, v43
	v_fmac_f32_e32 v253, v219, v253
	v_exp_f32_e32 v224, v47
	v_fmac_f32_e32 v254, v220, v254
	v_mfma_f32_32x32x16_bf16 v[82:97], v[66:69], v[174:177], v[82:97]
	ds_read_b128 v[154:157], v210 offset:6144
	ds_read_b128 v[158:161], v210 offset:7168
	v_rcp_f32_e32 v217, v251
	v_add_f32_e32 v221, 1.0, v221
	v_rcp_f32_e32 v218, v252
	v_add_f32_e32 v222, 1.0, v222
	v_rcp_f32_e32 v219, v253
	v_add_f32_e32 v223, 1.0, v223
	v_rcp_f32_e32 v220, v254
	v_add_f32_e32 v224, 1.0, v224
	v_mfma_f32_32x32x16_bf16 v[82:97], v[62:65], v[178:181], v[82:97]
	v_rcp_f32_e32 v221, v221
	v_fma_f32 v240, -v212, v217, v217
	v_rcp_f32_e32 v222, v222
	v_fma_f32 v241, -v213, v218, v218
	v_rcp_f32_e32 v223, v223
	v_fma_f32 v242, -v214, v219, v219
	v_rcp_f32_e32 v224, v224
	v_fma_f32 v243, -v215, v220, v220
	v_mfma_f32_32x32x16_bf16 v[82:97], v[58:61], v[182:185], v[82:97]
	v_exp_f32_e32 v246, v37
	v_fma_f32 v202, v221, v202, v240
	v_exp_f32_e32 v247, v41
	v_fma_f32 v203, v222, v203, v241
	v_exp_f32_e32 v248, v45
	v_fma_f32 v204, v223, v204, v242
	v_exp_f32_e32 v249, v49
	v_fma_f32 v205, v224, v205, v243
	v_mfma_f32_32x32x16_bf16 v[82:97], v[54:57], v[186:189], v[82:97]
	v_exp_f32_e32 v212, v202
	v_add_f32_e32 v246, 1.0, v246
	v_exp_f32_e32 v213, v203
	v_add_f32_e32 v247, 1.0, v247
	v_exp_f32_e32 v214, v204
	v_add_f32_e32 v248, 1.0, v248
	v_exp_f32_e32 v215, v205
	v_add_f32_e32 v249, 1.0, v249
	v_fmac_f32_e32 v246, v246, v212
	v_fmac_f32_e32 v247, v247, v213
	v_fmac_f32_e32 v248, v248, v214
	v_fmac_f32_e32 v249, v249, v215
	v_mfma_f32_32x32x16_bf16 v[82:97], v[50:53], v[190:193], v[82:97]
	v_rcp_f32_e32 v246, v246
	v_rcp_f32_e32 v247, v247
	v_rcp_f32_e32 v248, v248
	v_rcp_f32_e32 v249, v249
	v_fma_f32 v246, -v212, v246, v246
	v_fma_f32 v247, -v213, v247, v247
	v_fma_f32 v248, -v214, v248, v248
	v_fma_f32 v249, -v215, v249, v249
	v_cvt_pk_bf16_f32 v236, v246, v247
	v_cvt_pk_bf16_f32 v237, v248, v249
	s_waitcnt lgkmcnt(0)
	v_mfma_f32_32x32x16_bf16 v[2:17], v[126:129], v[130:133], v[2:17]
	v_add_u32_e32 v234, v231, v245
	ds_read_b128 v[34:37], v234 offset:0
	ds_read_b128 v[38:41], v234 offset:16
	ds_read_b128 v[42:45], v234 offset:32
	ds_read_b128 v[46:49], v234 offset:48
	v_add_u32_e32 v232, 0x100, v232
	v_exp_f32_e32 v212, v84
	v_exp_f32_e32 v213, v88
	v_exp_f32_e32 v214, v92
	v_exp_f32_e32 v215, v96
	v_mfma_f32_32x32x16_bf16 v[2:17], v[122:125], v[134:137], v[2:17]
	v_exp_f32_e32 v217, v82
	v_fma_f32 v251, v212, s12, s12
	v_exp_f32_e32 v218, v86
	v_fma_f32 v252, v213, s12, s12
	v_exp_f32_e32 v219, v90
	v_fma_f32 v253, v214, s12, s12
	v_exp_f32_e32 v220, v94
	v_fma_f32 v254, v215, s12, s12
	v_mfma_f32_32x32x16_bf16 v[2:17], v[118:121], v[138:141], v[2:17]
	v_exp_f32_e32 v221, v83
	v_fmac_f32_e32 v251, v217, v251
	v_exp_f32_e32 v222, v87
	v_fmac_f32_e32 v252, v218, v252
	v_exp_f32_e32 v223, v91
	v_fmac_f32_e32 v253, v219, v253
	v_exp_f32_e32 v224, v95
	v_fmac_f32_e32 v254, v220, v254
	v_mfma_f32_32x32x16_bf16 v[2:17], v[114:117], v[142:145], v[2:17]
	v_rcp_f32_e32 v217, v251
	v_add_f32_e32 v221, 1.0, v221
	v_rcp_f32_e32 v218, v252
	v_add_f32_e32 v222, 1.0, v222
	v_rcp_f32_e32 v219, v253
	v_add_f32_e32 v223, 1.0, v223
	v_rcp_f32_e32 v220, v254
	v_add_f32_e32 v224, 1.0, v224
	v_mfma_f32_32x32x16_bf16 v[2:17], v[110:113], v[146:149], v[2:17]
	v_rcp_f32_e32 v221, v221
	v_fma_f32 v240, -v212, v217, v217
	v_rcp_f32_e32 v222, v222
	v_fma_f32 v241, -v213, v218, v218
	v_rcp_f32_e32 v223, v223
	v_fma_f32 v242, -v214, v219, v219
	v_rcp_f32_e32 v224, v224
	v_fma_f32 v243, -v215, v220, v220
	v_mfma_f32_32x32x16_bf16 v[2:17], v[106:109], v[150:153], v[2:17]
	v_exp_f32_e32 v246, v85
	v_fma_f32 v206, v221, v206, v240
	v_exp_f32_e32 v247, v89
	v_fma_f32 v207, v222, v207, v241
	v_exp_f32_e32 v248, v93
	v_fma_f32 v208, v223, v208, v242
	v_exp_f32_e32 v249, v97
	v_fma_f32 v209, v224, v209, v243
	v_mfma_f32_32x32x16_bf16 v[2:17], v[102:105], v[154:157], v[2:17]
	v_exp_f32_e32 v212, v206
	v_add_f32_e32 v246, 1.0, v246
	v_exp_f32_e32 v213, v207
	v_add_f32_e32 v247, 1.0, v247
	v_exp_f32_e32 v214, v208
	v_add_f32_e32 v248, 1.0, v248
	v_exp_f32_e32 v215, v209
	v_add_f32_e32 v249, 1.0, v249
	v_fmac_f32_e32 v246, v246, v212
	v_fmac_f32_e32 v247, v247, v213
	v_fmac_f32_e32 v248, v248, v214
	v_fmac_f32_e32 v249, v249, v215
	v_mfma_f32_32x32x16_bf16 v[2:17], v[98:101], v[158:161], v[2:17]
	v_rcp_f32_e32 v246, v246
	v_rcp_f32_e32 v247, v247
	v_rcp_f32_e32 v248, v248
	v_rcp_f32_e32 v249, v249
	v_fma_f32 v246, -v212, v246, v246
	v_fma_f32 v247, -v213, v247, v247
	v_fma_f32 v248, -v214, v248, v248
	v_fma_f32 v249, -v215, v249, v249
	v_cvt_pk_bf16_f32 v238, v246, v247
	v_cvt_pk_bf16_f32 v239, v248, v249
	ds_write_b128 v211, v[236:239] offset:8192
	s_waitcnt lgkmcnt(0)
	s_barrier
	s_sub_u32 s16, s16, 1
	s_cmp_lg_u32 s16, 0
	s_cbranch_scc1 .Llight_loop
	v_mfma_f32_32x32x16_bf16 v[18:33], v[78:81], v[130:133], v[18:33]
	ds_read_b128 v[162:165], v210 offset:8192
	ds_read_b128 v[166:169], v210 offset:9216
	ds_read_b128 v[82:85], v234 offset:128
	ds_read_b128 v[86:89], v234 offset:144
	ds_read_b128 v[90:93], v234 offset:160
	ds_read_b128 v[94:97], v234 offset:176
	v_exp_f32_e32 v212, v4
	v_exp_f32_e32 v213, v8
	v_exp_f32_e32 v214, v12
	v_exp_f32_e32 v215, v16
	v_mfma_f32_32x32x16_bf16 v[18:33], v[74:77], v[134:137], v[18:33]
	ds_read_b128 v[170:173], v210 offset:10240
	ds_read_b128 v[174:177], v210 offset:11264
	v_exp_f32_e32 v217, v2
	v_fma_f32 v251, v212, s12, s12
	v_exp_f32_e32 v218, v6
	v_fma_f32 v252, v213, s12, s12
	v_exp_f32_e32 v219, v10
	v_fma_f32 v253, v214, s12, s12
	v_exp_f32_e32 v220, v14
	v_fma_f32 v254, v215, s12, s12
	v_mfma_f32_32x32x16_bf16 v[18:33], v[70:73], v[138:141], v[18:33]
	ds_read_b128 v[178:181], v210 offset:12288
	ds_read_b128 v[182:185], v210 offset:13312
	v_exp_f32_e32 v221, v3
	v_fmac_f32_e32 v251, v217, v251
	v_exp_f32_e32 v222, v7
	v_fmac_f32_e32 v252, v218, v252
	v_exp_f32_e32 v223, v11
	v_fmac_f32_e32 v253, v219, v253
	v_exp_f32_e32 v224, v15
	v_fmac_f32_e32 v254, v220, v254
	v_mfma_f32_32x32x16_bf16 v[18:33], v[66:69], v[142:145], v[18:33]
	ds_read_b128 v[186:189], v210 offset:14336
	ds_read_b128 v[190:193], v210 offset:15360
	v_rcp_f32_e32 v217, v251
	v_add_f32_e32 v221, 1.0, v221
	v_rcp_f32_e32 v218, v252
	v_add_f32_e32 v222, 1.0, v222
	v_rcp_f32_e32 v219, v253
	v_add_f32_e32 v223, 1.0, v223
	v_rcp_f32_e32 v220, v254
	v_add_f32_e32 v224, 1.0, v224
	v_mfma_f32_32x32x16_bf16 v[18:33], v[62:65], v[146:149], v[18:33]
	v_rcp_f32_e32 v221, v221
	v_fma_f32 v240, -v212, v217, v217
	v_rcp_f32_e32 v222, v222
	v_fma_f32 v241, -v213, v218, v218
	v_rcp_f32_e32 v223, v223
	v_fma_f32 v242, -v214, v219, v219
	v_rcp_f32_e32 v224, v224
	v_fma_f32 v243, -v215, v220, v220
	v_mfma_f32_32x32x16_bf16 v[18:33], v[58:61], v[150:153], v[18:33]
	v_exp_f32_e32 v246, v5
	v_fma_f32 v194, v221, v194, v240
	v_exp_f32_e32 v247, v9
	v_fma_f32 v195, v222, v195, v241
	v_exp_f32_e32 v248, v13
	v_fma_f32 v196, v223, v196, v242
	v_exp_f32_e32 v249, v17
	v_fma_f32 v197, v224, v197, v243
	v_mfma_f32_32x32x16_bf16 v[18:33], v[54:57], v[154:157], v[18:33]
	v_exp_f32_e32 v212, v194
	v_add_f32_e32 v246, 1.0, v246
	v_exp_f32_e32 v213, v195
	v_add_f32_e32 v247, 1.0, v247
	v_exp_f32_e32 v214, v196
	v_add_f32_e32 v248, 1.0, v248
	v_exp_f32_e32 v215, v197
	v_add_f32_e32 v249, 1.0, v249
	v_fmac_f32_e32 v246, v246, v212
	v_fmac_f32_e32 v247, v247, v213
	v_fmac_f32_e32 v248, v248, v214
	v_fmac_f32_e32 v249, v249, v215
	v_mfma_f32_32x32x16_bf16 v[18:33], v[50:53], v[158:161], v[18:33]
	v_rcp_f32_e32 v246, v246
	v_rcp_f32_e32 v247, v247
	v_rcp_f32_e32 v248, v248
	v_rcp_f32_e32 v249, v249
	v_fma_f32 v246, -v212, v246, v246
	v_fma_f32 v247, -v213, v247, v247
	v_fma_f32 v248, -v214, v248, v248
	v_fma_f32 v249, -v215, v249, v249
	v_cvt_pk_bf16_f32 v236, v246, v247
	v_cvt_pk_bf16_f32 v237, v248, v249
	s_waitcnt lgkmcnt(0)
	v_mfma_f32_32x32x16_bf16 v[34:49], v[126:129], v[162:165], v[34:49]
	v_exp_f32_e32 v212, v20
	v_exp_f32_e32 v213, v24
	v_exp_f32_e32 v214, v28
	v_exp_f32_e32 v215, v32
	v_mfma_f32_32x32x16_bf16 v[34:49], v[122:125], v[166:169], v[34:49]
	v_exp_f32_e32 v217, v18
	v_fma_f32 v251, v212, s12, s12
	v_exp_f32_e32 v218, v22
	v_fma_f32 v252, v213, s12, s12
	v_exp_f32_e32 v219, v26
	v_fma_f32 v253, v214, s12, s12
	v_exp_f32_e32 v220, v30
	v_fma_f32 v254, v215, s12, s12
	v_mfma_f32_32x32x16_bf16 v[34:49], v[118:121], v[170:173], v[34:49]
	v_exp_f32_e32 v221, v19
	v_fmac_f32_e32 v251, v217, v251
	v_exp_f32_e32 v222, v23
	v_fmac_f32_e32 v252, v218, v252
	v_exp_f32_e32 v223, v27
	v_fmac_f32_e32 v253, v219, v253
	v_exp_f32_e32 v224, v31
	v_fmac_f32_e32 v254, v220, v254
	v_mfma_f32_32x32x16_bf16 v[34:49], v[114:117], v[174:177], v[34:49]
	v_rcp_f32_e32 v217, v251
	v_add_f32_e32 v221, 1.0, v221
	v_rcp_f32_e32 v218, v252
	v_add_f32_e32 v222, 1.0, v222
	v_rcp_f32_e32 v219, v253
	v_add_f32_e32 v223, 1.0, v223
	v_rcp_f32_e32 v220, v254
	v_add_f32_e32 v224, 1.0, v224
	v_mfma_f32_32x32x16_bf16 v[34:49], v[110:113], v[178:181], v[34:49]
	v_rcp_f32_e32 v221, v221
	v_fma_f32 v240, -v212, v217, v217
	v_rcp_f32_e32 v222, v222
	v_fma_f32 v241, -v213, v218, v218
	v_rcp_f32_e32 v223, v223
	v_fma_f32 v242, -v214, v219, v219
	v_rcp_f32_e32 v224, v224
	v_fma_f32 v243, -v215, v220, v220
	v_mfma_f32_32x32x16_bf16 v[34:49], v[106:109], v[182:185], v[34:49]
	v_exp_f32_e32 v246, v21
	v_fma_f32 v198, v221, v198, v240
	v_exp_f32_e32 v247, v25
	v_fma_f32 v199, v222, v199, v241
	v_exp_f32_e32 v248, v29
	v_fma_f32 v200, v223, v200, v242
	v_exp_f32_e32 v249, v33
	v_fma_f32 v201, v224, v201, v243
	v_mfma_f32_32x32x16_bf16 v[34:49], v[102:105], v[186:189], v[34:49]
	v_exp_f32_e32 v212, v198
	v_add_f32_e32 v246, 1.0, v246
	v_exp_f32_e32 v213, v199
	v_add_f32_e32 v247, 1.0, v247
	v_exp_f32_e32 v214, v200
	v_add_f32_e32 v248, 1.0, v248
	v_exp_f32_e32 v215, v201
	v_add_f32_e32 v249, 1.0, v249
	v_fmac_f32_e32 v246, v246, v212
	v_fmac_f32_e32 v247, v247, v213
	v_fmac_f32_e32 v248, v248, v214
	v_fmac_f32_e32 v249, v249, v215
	v_mfma_f32_32x32x16_bf16 v[34:49], v[98:101], v[190:193], v[34:49]
	v_rcp_f32_e32 v246, v246
	v_rcp_f32_e32 v247, v247
	v_rcp_f32_e32 v248, v248
	v_rcp_f32_e32 v249, v249
	v_fma_f32 v246, -v212, v246, v246
	v_fma_f32 v247, -v213, v247, v247
	v_fma_f32 v248, -v214, v248, v248
	v_fma_f32 v249, -v215, v249, v249
	v_cvt_pk_bf16_f32 v238, v246, v247
	v_cvt_pk_bf16_f32 v239, v248, v249
	ds_write_b128 v211, v[236:239] offset:0
	s_waitcnt lgkmcnt(0)
	s_barrier
	s_bfe_u32 s20, s19, 0x10006
	s_lshl_b32 s21, s20, 7
	s_lshl_b32 s20, s20, 13
	s_add_u32 s20, s20, 0x30000
	s_add_u32 s22, s14, s20
	s_addc_u32 s23, s15, 0
	s_add_u32 s24, s22, 0x1000
	s_addc_u32 s25, s23, 0
	global_load_dwordx4 v[98:101], v210, s[22:23] offset:0
	global_load_dwordx4 v[102:105], v210, s[22:23] offset:1024
	global_load_dwordx4 v[106:109], v210, s[22:23] offset:2048
	global_load_dwordx4 v[110:113], v210, s[22:23] offset:3072
	global_load_dwordx4 v[114:117], v210, s[24:25] offset:0
	global_load_dwordx4 v[118:121], v210, s[24:25] offset:1024
	global_load_dwordx4 v[122:125], v210, s[24:25] offset:2048
	global_load_dwordx4 v[126:129], v210, s[24:25] offset:3072
	v_or_b32_e32 v250, s21, v230
	global_load_dwordx4 v[130:133], v250, s[4:5] offset:0
	global_load_dwordx4 v[134:137], v250, s[4:5] offset:32
	global_load_dwordx4 v[138:141], v250, s[4:5] offset:64
	global_load_dwordx4 v[142:145], v250, s[4:5] offset:96
	global_load_dwordx4 v[146:149], v250, s[6:7] offset:0
	global_load_dwordx4 v[150:153], v250, s[6:7] offset:32
	global_load_dwordx4 v[154:157], v250, s[6:7] offset:64
	global_load_dwordx4 v[158:161], v250, s[6:7] offset:96
	s_load_dword s26, s[8:9], 0x0
	v_mfma_f32_32x32x16_bf16 v[82:97], v[78:81], v[162:165], v[82:97]
	v_exp_f32_e32 v212, v36
	v_exp_f32_e32 v213, v40
	v_exp_f32_e32 v214, v44
	v_exp_f32_e32 v215, v48
	v_mfma_f32_32x32x16_bf16 v[82:97], v[74:77], v[166:169], v[82:97]
	v_exp_f32_e32 v217, v34
	v_fma_f32 v251, v212, s12, s12
	v_exp_f32_e32 v218, v38
	v_fma_f32 v252, v213, s12, s12
	v_exp_f32_e32 v219, v42
	v_fma_f32 v253, v214, s12, s12
	v_exp_f32_e32 v220, v46
	v_fma_f32 v254, v215, s12, s12
	v_mfma_f32_32x32x16_bf16 v[82:97], v[70:73], v[170:173], v[82:97]
	v_exp_f32_e32 v221, v35
	v_fmac_f32_e32 v251, v217, v251
	v_exp_f32_e32 v222, v39
	v_fmac_f32_e32 v252, v218, v252
	v_exp_f32_e32 v223, v43
	v_fmac_f32_e32 v253, v219, v253
	v_exp_f32_e32 v224, v47
	v_fmac_f32_e32 v254, v220, v254
	v_mfma_f32_32x32x16_bf16 v[82:97], v[66:69], v[174:177], v[82:97]
	v_rcp_f32_e32 v217, v251
	v_add_f32_e32 v221, 1.0, v221
	v_rcp_f32_e32 v218, v252
	v_add_f32_e32 v222, 1.0, v222
	v_rcp_f32_e32 v219, v253
	v_add_f32_e32 v223, 1.0, v223
	v_rcp_f32_e32 v220, v254
	v_add_f32_e32 v224, 1.0, v224
	v_mfma_f32_32x32x16_bf16 v[82:97], v[62:65], v[178:181], v[82:97]
	v_rcp_f32_e32 v221, v221
	v_fma_f32 v240, -v212, v217, v217
	v_rcp_f32_e32 v222, v222
	v_fma_f32 v241, -v213, v218, v218
	v_rcp_f32_e32 v223, v223
	v_fma_f32 v242, -v214, v219, v219
	v_rcp_f32_e32 v224, v224
	v_fma_f32 v243, -v215, v220, v220
	v_mfma_f32_32x32x16_bf16 v[82:97], v[58:61], v[182:185], v[82:97]
	v_exp_f32_e32 v246, v37
	v_fma_f32 v202, v221, v202, v240
	v_exp_f32_e32 v247, v41
	v_fma_f32 v203, v222, v203, v241
	v_exp_f32_e32 v248, v45
	v_fma_f32 v204, v223, v204, v242
	v_exp_f32_e32 v249, v49
	v_fma_f32 v205, v224, v205, v243
	v_mfma_f32_32x32x16_bf16 v[82:97], v[54:57], v[186:189], v[82:97]
	v_exp_f32_e32 v212, v202
	v_add_f32_e32 v246, 1.0, v246
	v_exp_f32_e32 v213, v203
	v_add_f32_e32 v247, 1.0, v247
	v_exp_f32_e32 v214, v204
	v_add_f32_e32 v248, 1.0, v248
	v_exp_f32_e32 v215, v205
	v_add_f32_e32 v249, 1.0, v249
	v_fmac_f32_e32 v246, v246, v212
	v_fmac_f32_e32 v247, v247, v213
	v_fmac_f32_e32 v248, v248, v214
	v_fmac_f32_e32 v249, v249, v215
	v_mfma_f32_32x32x16_bf16 v[82:97], v[50:53], v[190:193], v[82:97]
	v_rcp_f32_e32 v246, v246
	v_rcp_f32_e32 v247, v247
	v_rcp_f32_e32 v248, v248
	v_rcp_f32_e32 v249, v249
	v_fma_f32 v246, -v212, v246, v246
	v_fma_f32 v247, -v213, v247, v247
	v_fma_f32 v248, -v214, v248, v248
	v_fma_f32 v249, -v215, v249, v249
	v_cvt_pk_bf16_f32 v236, v246, v247
	v_cvt_pk_bf16_f32 v237, v248, v249
	s_waitcnt lgkmcnt(0)
	v_exp_f32_e32 v212, v84
	v_exp_f32_e32 v213, v88
	v_exp_f32_e32 v214, v92
	v_exp_f32_e32 v215, v96
	v_exp_f32_e32 v217, v82
	v_fma_f32 v251, v212, s12, s12
	v_exp_f32_e32 v218, v86
	v_fma_f32 v252, v213, s12, s12
	v_exp_f32_e32 v219, v90
	v_fma_f32 v253, v214, s12, s12
	v_exp_f32_e32 v220, v94
	v_fma_f32 v254, v215, s12, s12
	v_exp_f32_e32 v221, v83
	v_fmac_f32_e32 v251, v217, v251
	v_exp_f32_e32 v222, v87
	v_fmac_f32_e32 v252, v218, v252
	v_exp_f32_e32 v223, v91
	v_fmac_f32_e32 v253, v219, v253
	v_exp_f32_e32 v224, v95
	v_fmac_f32_e32 v254, v220, v254
	v_rcp_f32_e32 v217, v251
	v_add_f32_e32 v221, 1.0, v221
	v_rcp_f32_e32 v218, v252
	v_add_f32_e32 v222, 1.0, v222
	v_rcp_f32_e32 v219, v253
	v_add_f32_e32 v223, 1.0, v223
	v_rcp_f32_e32 v220, v254
	v_add_f32_e32 v224, 1.0, v224
	v_rcp_f32_e32 v221, v221
	v_fma_f32 v240, -v212, v217, v217
	v_rcp_f32_e32 v222, v222
	v_fma_f32 v241, -v213, v218, v218
	v_rcp_f32_e32 v223, v223
	v_fma_f32 v242, -v214, v219, v219
	v_rcp_f32_e32 v224, v224
	v_fma_f32 v243, -v215, v220, v220
	v_exp_f32_e32 v246, v85
	v_fma_f32 v206, v221, v206, v240
	v_exp_f32_e32 v247, v89
	v_fma_f32 v207, v222, v207, v241
	v_exp_f32_e32 v248, v93
	v_fma_f32 v208, v223, v208, v242
	v_exp_f32_e32 v249, v97
	v_fma_f32 v209, v224, v209, v243
	v_exp_f32_e32 v212, v206
	v_add_f32_e32 v246, 1.0, v246
	v_exp_f32_e32 v213, v207
	v_add_f32_e32 v247, 1.0, v247
	v_exp_f32_e32 v214, v208
	v_add_f32_e32 v248, 1.0, v248
	v_exp_f32_e32 v215, v209
	v_add_f32_e32 v249, 1.0, v249
	v_fmac_f32_e32 v246, v246, v212
	v_fmac_f32_e32 v247, v247, v213
	v_fmac_f32_e32 v248, v248, v214
	v_fmac_f32_e32 v249, v249, v215
	v_rcp_f32_e32 v246, v246
	v_rcp_f32_e32 v247, v247
	v_rcp_f32_e32 v248, v248
	v_rcp_f32_e32 v249, v249
	v_fma_f32 v246, -v212, v246, v246
	v_fma_f32 v247, -v213, v247, v247
	v_fma_f32 v248, -v214, v248, v248
	v_fma_f32 v249, -v215, v249, v249
	v_cvt_pk_bf16_f32 v238, v246, v247
	v_cvt_pk_bf16_f32 v239, v248, v249
	ds_write_b128 v211, v[236:239] offset:8192
	s_waitcnt lgkmcnt(0)
	s_barrier
	s_lshl_b32 s20, s19, 6
	s_and_b32 s20, s20, 0x2000
	v_or_b32_e32 v20, s20, v210
	ds_read_b128 v[162:165], v20 offset:0
	ds_read_b128 v[166:169], v20 offset:1024
	ds_read_b128 v[170:173], v20 offset:2048
	ds_read_b128 v[174:177], v20 offset:3072
	ds_read_b128 v[178:181], v20 offset:4096
	ds_read_b128 v[182:185], v20 offset:5120
	ds_read_b128 v[186:189], v20 offset:6144
	ds_read_b128 v[190:193], v20 offset:7168
	s_bfe_u32 s20, s19, 0x10006
	s_lshl_b32 s20, s20, 9
	s_and_b32 s21, s19, 0x80
	s_or_b32 s20, s20, s21
	v_lshlrev_b32_e32 v19, 2, v229
	v_add3_u32 v19, s20, v19, v228
	s_waitcnt vmcnt(0)
	s_waitcnt lgkmcnt(7)
	v_mfma_f32_32x32x16_bf16 v[2:17], v[98:101], v[162:165], 0
	s_waitcnt lgkmcnt(6)
	v_mfma_f32_32x32x16_bf16 v[2:17], v[102:105], v[166:169], v[2:17]
	s_waitcnt lgkmcnt(5)
	v_mfma_f32_32x32x16_bf16 v[2:17], v[106:109], v[170:173], v[2:17]
	s_waitcnt lgkmcnt(4)
	v_mfma_f32_32x32x16_bf16 v[2:17], v[110:113], v[174:177], v[2:17]
	s_waitcnt lgkmcnt(3)
	v_mfma_f32_32x32x16_bf16 v[2:17], v[114:117], v[178:181], v[2:17]
	s_waitcnt lgkmcnt(2)
	v_mfma_f32_32x32x16_bf16 v[2:17], v[118:121], v[182:185], v[2:17]
	s_waitcnt lgkmcnt(1)
	v_mfma_f32_32x32x16_bf16 v[2:17], v[122:125], v[186:189], v[2:17]
	s_waitcnt lgkmcnt(0)
	v_mfma_f32_32x32x16_bf16 v[2:17], v[126:129], v[190:193], v[2:17]
	s_nop 15
	s_nop 3
	v_add_f32_e32 v2, v2, v130
	v_add_f32_e32 v3, v3, v131
	v_add_f32_e32 v4, v4, v132
	v_add_f32_e32 v5, v5, v133
	v_add_f32_e32 v6, v6, v134
	v_add_f32_e32 v7, v7, v135
	v_add_f32_e32 v8, v8, v136
	v_add_f32_e32 v9, v9, v137
	v_add_f32_e32 v10, v10, v138
	v_add_f32_e32 v11, v11, v139
	v_add_f32_e32 v12, v12, v140
	v_add_f32_e32 v13, v13, v141
	v_add_f32_e32 v14, v14, v142
	v_add_f32_e32 v15, v15, v143
	v_add_f32_e32 v16, v16, v144
	v_add_f32_e32 v17, v17, v145
	v_max_f32_e32 v2, 0, v2
	v_max_f32_e32 v3, 0, v3
	v_max_f32_e32 v4, 0, v4
	v_max_f32_e32 v5, 0, v5
	v_max_f32_e32 v6, 0, v6
	v_max_f32_e32 v7, 0, v7
	v_max_f32_e32 v8, 0, v8
	v_max_f32_e32 v9, 0, v9
	v_max_f32_e32 v10, 0, v10
	v_max_f32_e32 v11, 0, v11
	v_max_f32_e32 v12, 0, v12
	v_max_f32_e32 v13, 0, v13
	v_max_f32_e32 v14, 0, v14
	v_max_f32_e32 v15, 0, v15
	v_max_f32_e32 v16, 0, v16
	v_max_f32_e32 v17, 0, v17
	v_fma_f32 v18, v2, v146, 0
	v_fmac_f32_e32 v18, v3, v147
	v_fmac_f32_e32 v18, v4, v148
	v_fmac_f32_e32 v18, v5, v149
	v_fmac_f32_e32 v18, v6, v150
	v_fmac_f32_e32 v18, v7, v151
	v_fmac_f32_e32 v18, v8, v152
	v_fmac_f32_e32 v18, v9, v153
	v_fmac_f32_e32 v18, v10, v154
	v_fmac_f32_e32 v18, v11, v155
	v_fmac_f32_e32 v18, v12, v156
	v_fmac_f32_e32 v18, v13, v157
	v_fmac_f32_e32 v18, v14, v158
	v_fmac_f32_e32 v18, v15, v159
	v_fmac_f32_e32 v18, v16, v160
	v_fmac_f32_e32 v18, v17, v161
	ds_write_b32 v19, v18 offset:35904
	s_branch .LBB1_40
